# SWA unit: Q fragments of sub-blocks 1-3 prefetched by sub-block 0 (constant row stride) and copied over instead of a load-wait per sub-block; on top of V staging prefetch
# baseline (speedup 1.0000x reference)
; __device__ __forceinline__ void swa_unit(Frame& F, const bf16_t* proj, const float* sinks, unsigned char* Y, int b, int kvh, int qb) {
;     ...
;     for (int sb = 0; sb < 4; ++sb) {
;         const int t = qb * 128 + sb * 32 + r32;
;         bf16x8 qf[4];
;         { const bf16_t* qrow = proj + (rb + t) * NIN + C_SQ + hq * 64 + hh * 8;
; #pragma unroll
;           for (int s = 0; s < 4; ++s) qf[s] = *(const bf16x8*)(qrow + s * 16); }
;         State st; init(st);
;         int kt0 = sb; if (qb == 0 && kt0 < 4) kt0 = 4;
;         if (kt0 == sb) tile<2>(lds, sb, qf, st, lane);
.LBB0_907:
	s_lshl_b32 s72, s71, 5
	v_add_u32_e32 v1, s72, v156
	v_or_b32_e32 v146, s46, v1
	v_mov_b64_e32 v[4:5], s[58:59]
	v_mad_u64_u32 v[4:5], s[52:53], v146, s54, v[4:5]
	v_mad_i32_i24 v5, s47, v152, v5
	v_lshl_add_u64 v[4:5], v[4:5], 0, s[0:1]
	v_lshl_add_u64 v[4:5], v[140:141], 1, v[4:5]
	s_mov_b64 s[52:53], 0x1c00
	v_lshl_add_u64 v[6:7], v[4:5], 0, s[52:53]
	v_add_co_u32_e32 v4, vcc, 0x1000, v4
	s_and_b64 s[52:53], exec, s[44:45]
	s_nop 0
	v_addc_co_u32_e32 v5, vcc, 0, v5, vcc
	s_cselect_b32 s73, 4, s71
	s_cmp_lg_u32 s71, 0
	s_cbranch_scc1 .Lswq1_sel
	global_load_dwordx4 v[122:125], v[6:7], off offset:32
	global_load_dwordx4 v[118:121], v[6:7], off offset:64
	global_load_dwordx4 v[126:129], v[4:5], off offset:3072
	global_load_dwordx4 v[114:117], v[6:7], off offset:96
	s_mov_b64 s[52:53], 0x4c000
	v_lshl_add_u64 v[200:201], v[6:7], 0, s[52:53]
	v_lshl_add_u64 v[234:235], v[4:5], 0, s[52:53]
	global_load_dwordx4 v[186:189], v[200:201], off offset:32
	global_load_dwordx4 v[190:193], v[200:201], off offset:64
	global_load_dwordx4 v[196:199], v[234:235], off offset:3072
	global_load_dwordx4 v[210:213], v[200:201], off offset:96
	s_add_u32 s52, s52, 0x4c000
	v_lshl_add_u64 v[200:201], v[6:7], 0, s[52:53]
	v_lshl_add_u64 v[234:235], v[4:5], 0, s[52:53]
	global_load_dwordx4 v[214:217], v[200:201], off offset:32
	global_load_dwordx4 v[218:221], v[200:201], off offset:64
	global_load_dwordx4 v[222:225], v[234:235], off offset:3072
	global_load_dwordx4 v[230:233], v[200:201], off offset:96
	s_add_u32 s52, s52, 0x4c000
	v_lshl_add_u64 v[200:201], v[6:7], 0, s[52:53]
	v_lshl_add_u64 v[234:235], v[4:5], 0, s[52:53]
	global_load_dwordx4 v[238:241], v[200:201], off offset:32
	global_load_dwordx4 v[242:245], v[200:201], off offset:64
	global_load_dwordx4 v[246:249], v[234:235], off offset:3072
	global_load_dwordx4 v[250:253], v[200:201], off offset:96
	s_branch .Lswq1_done
.Lswq1_sel:
	s_waitcnt vmcnt(4)
	s_cmp_eq_u32 s71, 1
	s_cbranch_scc0 .Lswq1_c2
	v_mov_b64_e32 v[122:123], v[186:187]
	v_mov_b64_e32 v[124:125], v[188:189]
	v_mov_b64_e32 v[118:119], v[190:191]
	v_mov_b64_e32 v[120:121], v[192:193]
	v_mov_b64_e32 v[126:127], v[196:197]
	v_mov_b64_e32 v[128:129], v[198:199]
	v_mov_b64_e32 v[114:115], v[210:211]
	v_mov_b64_e32 v[116:117], v[212:213]
	s_branch .Lswq1_done
.Lswq1_c2:
	s_cmp_eq_u32 s71, 2
	s_cbranch_scc0 .Lswq1_c3
	v_mov_b64_e32 v[122:123], v[214:215]
	v_mov_b64_e32 v[124:125], v[216:217]
	v_mov_b64_e32 v[118:119], v[218:219]
	v_mov_b64_e32 v[120:121], v[220:221]
	v_mov_b64_e32 v[126:127], v[222:223]
	v_mov_b64_e32 v[128:129], v[224:225]
	v_mov_b64_e32 v[114:115], v[230:231]
	v_mov_b64_e32 v[116:117], v[232:233]
	s_branch .Lswq1_done
.Lswq1_c3:
	v_mov_b64_e32 v[122:123], v[238:239]
	v_mov_b64_e32 v[124:125], v[240:241]
	v_mov_b64_e32 v[118:119], v[242:243]
	v_mov_b64_e32 v[120:121], v[244:245]
	v_mov_b64_e32 v[126:127], v[246:247]
	v_mov_b64_e32 v[128:129], v[248:249]
	v_mov_b64_e32 v[114:115], v[250:251]
	v_mov_b64_e32 v[116:117], v[252:253]
.Lswq1_done:
	v_mov_b32_e32 v147, s47
	s_cmp_eq_u32 s73, s71
	s_mov_b64 s[52:53], -1
	s_cbranch_scc1 .LBB0_909
	s_mov_b64 s[52:53], 0
.LBB0_909:
	s_andn2_b64 vcc, exec, s[52:53]
	s_cbranch_vccnz .LBB0_912
	v_or_b32_e32 v1, s72, v139
	v_mad_u64_u32 v[8:9], s[52:53], v1, s55, v[142:143]
	ds_read_b128 v[4:7], v8
	ds_read_b128 v[164:167], v8 offset:32
	ds_read_b128 v[168:171], v8 offset:64
	ds_read_b128 v[172:175], v8 offset:96
	s_waitcnt vmcnt(13) lgkmcnt(3)
	v_mfma_f32_32x32x16_bf16 v[66:81], v[4:7], v[126:129], v[34:49]
	s_waitcnt lgkmcnt(2)
	v_mfma_f32_32x32x16_bf16 v[66:81], v[164:167], v[122:125], v[66:81]
	s_waitcnt lgkmcnt(1)
	v_mfma_f32_32x32x16_bf16 v[66:81], v[168:171], v[118:121], v[66:81]
	s_waitcnt vmcnt(12) lgkmcnt(0)
	v_mfma_f32_32x32x16_bf16 v[66:81], v[172:175], v[114:117], v[66:81]
	s_nop 15
	s_nop 7
	s_nop 0
	v_max3_f32 v1, v66, v67, v68
	v_max3_f32 v3, v69, v70, v71
	v_max3_f32 v4, v72, v73, v74
	v_max3_f32 v5, v75, v76, v77
	v_max3_f32 v6, v78, v79, v80
	s_nop 0
	v_max3_f32 v1, v1, v3, v81
	v_max3_f32 v3, v4, v5, v6
	s_nop 0
	v_max_f32 v1, v1, v3
	s_nop 0
	v_mov_b32_e32 v3, v1
	s_nop 1
	v_permlane32_swap_b32_e32 v1, v3
	v_max_f32_e32 v3, v3, v3
	v_max_f32_e32 v1, v1, v1
	v_max_f32_e32 v1, v1, v3
	v_cmp_lt_f32_e32 vcc, s63, v1
	s_cbranch_vccz .LBB0_913
	s_nop 0
	v_cndmask_b32_e32 v4, 0, v1, vcc
	v_exp_f32_e64 v3, -v4
	v_sub_f32_e32 v82, 0x447a0000, v4
	v_add_f32_e32 v1, 0xc47a0000, v4
	v_pk_add_f32 v[66:67], v[66:67], v[4:5] op_sel_hi:[1,0] neg_lo:[0,1] neg_hi:[0,1]
	v_mul_f32_e32 v50, 0, v3
	v_pk_add_f32 v[68:69], v[68:69], v[4:5] op_sel_hi:[1,0] neg_lo:[0,1] neg_hi:[0,1]
	v_pk_add_f32 v[70:71], v[70:71], v[4:5] op_sel_hi:[1,0] neg_lo:[0,1] neg_hi:[0,1]
	v_pk_add_f32 v[72:73], v[72:73], v[4:5] op_sel_hi:[1,0] neg_lo:[0,1] neg_hi:[0,1]
	v_pk_add_f32 v[74:75], v[74:75], v[4:5] op_sel_hi:[1,0] neg_lo:[0,1] neg_hi:[0,1]
	v_pk_add_f32 v[76:77], v[76:77], v[4:5] op_sel_hi:[1,0] neg_lo:[0,1] neg_hi:[0,1]
	v_pk_add_f32 v[78:79], v[78:79], v[4:5] op_sel_hi:[1,0] neg_lo:[0,1] neg_hi:[0,1]
	v_pk_add_f32 v[80:81], v[80:81], v[4:5] op_sel_hi:[1,0] neg_lo:[0,1] neg_hi:[0,1]
	v_mov_b32_e32 v83, v82
	v_mov_b32_e32 v84, v82
	v_mov_b32_e32 v85, v82
	v_mov_b32_e32 v86, v82
	v_mov_b32_e32 v87, v82
	v_mov_b32_e32 v88, v82
	v_mov_b32_e32 v89, v82
	v_mov_b32_e32 v90, v82
	v_mov_b32_e32 v91, v82
	v_mov_b32_e32 v92, v82
	v_mov_b32_e32 v93, v82
	v_mov_b32_e32 v94, v82
	v_mov_b32_e32 v95, v82
	v_mov_b32_e32 v96, v82
	v_mov_b32_e32 v97, v82
	s_branch .LBB0_914

; #define LAS __attribute__((address_space(3)))
; __device__ __forceinline__ float xhalf_max(float v) { auto rr = __builtin_amdgcn_permlane32_swap(__float_as_uint(v), __float_as_uint(v), false, false); return fmaxf(__uint_as_float(rr[0]), __uint_as_float(rr[1])); }
; template <int MODE>
; __device__ __forceinline__ void tile(LAS unsigned char* lds, int kt, const bf16x8 (&qf)[4], State& st, int lane) {
;     const int r32 = lane & 31, h = lane >> 5;
;     f32x16 S;
;     if (MODE == 3) S = st.negm;
;     else {
; #pragma unroll
;         for (int r = 0; r < 16; ++r) { const int ko = (r & 3) + 8 * (r >> 2) + 4 * h; const bool ok = (MODE == 1) ? (ko <= r32) : (ko > r32); S[r] = ok ? st.negm[r] : NEG; } }
;     const LAS unsigned char* kp = lds + K_OFF + (kt * 32 + r32) * KROW + h * 16;
; #pragma unroll
;     for (int s = 0; s < 4; ++s) { const bf16x8 a = *(const LAS bf16x8*)(kp + s * 32); S = __builtin_amdgcn_mfma_f32_32x32x16_bf16(a, qf[s], S, 0, 0, 0); }
;     float tmax;
;     asm volatile("s_nop 15\n\ts_nop 7" : "+v"(S));
;     { float m0, m1, m2, m3, m4;
;       asm("v_max3_f32 %0, %1, %2, %3" : "=v"(m0) : "v"(S[0]), "v"(S[1]), "v"(S[2]));    asm("v_max3_f32 %0, %1, %2, %3" : "=v"(m1) : "v"(S[3]), "v"(S[4]), "v"(S[5]));
;       asm("v_max3_f32 %0, %1, %2, %3" : "=v"(m2) : "v"(S[6]), "v"(S[7]), "v"(S[8]));    asm("v_max3_f32 %0, %1, %2, %3" : "=v"(m3) : "v"(S[9]), "v"(S[10]), "v"(S[11]));
;       asm("v_max3_f32 %0, %1, %2, %3" : "=v"(m4) : "v"(S[12]), "v"(S[13]), "v"(S[14])); asm("v_max3_f32 %0, %1, %2, %3" : "=v"(m0) : "v"(m0), "v"(m1), "v"(S[15]));
;       asm("v_max3_f32 %0, %1, %2, %3" : "=v"(m2) : "v"(m2), "v"(m3), "v"(m4));          asm("v_max_f32 %0, %1, %2" : "=v"(tmax) : "v"(m0), "v"(m2)); }
;     tmax = xhalf_max(tmax);
;     if (__any(tmax > THR)) {
;         const float d = tmax > THR ? tmax : 0.f, alpha = __builtin_amdgcn_exp2f(-d);
;         st.m += d; st.l *= alpha;
; #pragma unroll
;         for (int r = 0; r < 16; ++r) { S[r] -= d; st.negm[r] -= d; st.o0[r] *= alpha; st.o1[r] *= alpha; }
;     }
.LBB0_918:
	ds_read_b128 v[6:9], v4
	ds_read_b128 v[164:167], v4 offset:32
	ds_read_b128 v[168:171], v4 offset:64
	ds_read_b128 v[172:175], v4 offset:96
	s_waitcnt vmcnt(13) lgkmcnt(3)
	v_mfma_f32_32x32x16_bf16 v[98:113], v[6:9], v[126:129], v[82:97]
	s_waitcnt lgkmcnt(2)
	v_mfma_f32_32x32x16_bf16 v[98:113], v[164:167], v[122:125], v[98:113]
	s_waitcnt lgkmcnt(1)
	v_mfma_f32_32x32x16_bf16 v[98:113], v[168:171], v[118:121], v[98:113]
	s_waitcnt vmcnt(12) lgkmcnt(0)
	v_mfma_f32_32x32x16_bf16 v[98:113], v[172:175], v[114:117], v[98:113]
	s_nop 15
	s_nop 7
	s_nop 0
	v_max3_f32 v5, v98, v99, v100
	v_max3_f32 v6, v101, v102, v103
	v_max3_f32 v7, v104, v105, v106
	v_max3_f32 v8, v107, v108, v109
	v_max3_f32 v9, v110, v111, v112
	s_nop 0
	v_max3_f32 v5, v5, v6, v113
	v_max3_f32 v6, v7, v8, v9
	s_nop 0
	v_max_f32 v5, v5, v6
	s_nop 0
	v_mov_b32_e32 v6, v5
	s_nop 1
	v_permlane32_swap_b32_e32 v5, v6
	v_max_f32_e32 v6, v6, v6
	v_max_f32_e32 v5, v5, v5
	v_max_f32_e32 v5, v5, v6
	v_cmp_lt_f32_e32 vcc, s63, v5
	s_cbranch_vccz .LBB0_917
	s_nop 0
	v_cndmask_b32_e32 v6, 0, v5, vcc
	v_exp_f32_e64 v8, -v6
	v_add_f32_e32 v1, v1, v6
	v_pk_add_f32 v[98:99], v[98:99], v[6:7] op_sel_hi:[1,0] neg_lo:[0,1] neg_hi:[0,1]
	v_pk_add_f32 v[100:101], v[100:101], v[6:7] op_sel_hi:[1,0] neg_lo:[0,1] neg_hi:[0,1]
	v_mul_f32_e32 v160, v160, v8
	v_pk_add_f32 v[102:103], v[102:103], v[6:7] op_sel_hi:[1,0] neg_lo:[0,1] neg_hi:[0,1]
	v_pk_add_f32 v[104:105], v[104:105], v[6:7] op_sel_hi:[1,0] neg_lo:[0,1] neg_hi:[0,1]
	v_pk_add_f32 v[106:107], v[106:107], v[6:7] op_sel_hi:[1,0] neg_lo:[0,1] neg_hi:[0,1]
	v_pk_add_f32 v[108:109], v[108:109], v[6:7] op_sel_hi:[1,0] neg_lo:[0,1] neg_hi:[0,1]
	v_pk_add_f32 v[110:111], v[110:111], v[6:7] op_sel_hi:[1,0] neg_lo:[0,1] neg_hi:[0,1]
	v_pk_add_f32 v[112:113], v[112:113], v[6:7] op_sel_hi:[1,0] neg_lo:[0,1] neg_hi:[0,1]
	v_sub_f32_e32 v97, v97, v6
	v_sub_f32_e32 v96, v96, v6
	v_sub_f32_e32 v95, v95, v6
	v_sub_f32_e32 v94, v94, v6
	v_sub_f32_e32 v93, v93, v6
	v_sub_f32_e32 v92, v92, v6
	v_sub_f32_e32 v91, v91, v6
	v_sub_f32_e32 v90, v90, v6
	v_sub_f32_e32 v89, v89, v6
	v_sub_f32_e32 v88, v88, v6
	v_sub_f32_e32 v87, v87, v6
	v_sub_f32_e32 v86, v86, v6
	v_sub_f32_e32 v85, v85, v6
	v_sub_f32_e32 v84, v84, v6
	v_sub_f32_e32 v83, v83, v6
	v_sub_f32_e32 v82, v82, v6
	v_pk_mul_f32 v[80:81], v[80:81], v[8:9] op_sel_hi:[1,0]
	v_pk_mul_f32 v[78:79], v[78:79], v[8:9] op_sel_hi:[1,0]
	v_pk_mul_f32 v[76:77], v[76:77], v[8:9] op_sel_hi:[1,0]
	v_pk_mul_f32 v[74:75], v[74:75], v[8:9] op_sel_hi:[1,0]
	v_pk_mul_f32 v[72:73], v[72:73], v[8:9] op_sel_hi:[1,0]
	v_pk_mul_f32 v[70:71], v[70:71], v[8:9] op_sel_hi:[1,0]
	v_pk_mul_f32 v[68:69], v[68:69], v[8:9] op_sel_hi:[1,0]
	v_pk_mul_f32 v[66:67], v[66:67], v[8:9] op_sel_hi:[1,0]
	v_pk_mul_f32 v[64:65], v[64:65], v[8:9] op_sel_hi:[1,0]
	v_pk_mul_f32 v[62:63], v[62:63], v[8:9] op_sel_hi:[1,0]
	v_pk_mul_f32 v[60:61], v[60:61], v[8:9] op_sel_hi:[1,0]
	v_pk_mul_f32 v[58:59], v[58:59], v[8:9] op_sel_hi:[1,0]
	v_pk_mul_f32 v[56:57], v[56:57], v[8:9] op_sel_hi:[1,0]
	v_pk_mul_f32 v[54:55], v[54:55], v[8:9] op_sel_hi:[1,0]
	v_pk_mul_f32 v[52:53], v[52:53], v[8:9] op_sel_hi:[1,0]
	v_pk_mul_f32 v[50:51], v[50:51], v[8:9] op_sel_hi:[1,0]
	s_branch .LBB0_917
.LBB0_920:
	v_lshl_or_b32 v3, s53, 5, v139
	v_mad_u64_u32 v[12:13], s[72:73], v3, s55, v[142:143]
	ds_read_b128 v[4:7], v12
	ds_read_b128 v[8:11], v12 offset:32
	v_cndmask_b32_e64 v82, v82, v153, s[8:9]
	v_cndmask_b32_e64 v83, v153, v83, s[10:11]
	v_cndmask_b32_e64 v84, v84, v153, s[12:13]
	v_cndmask_b32_e64 v85, v85, v153, s[14:15]
	v_cndmask_b32_e64 v86, v86, v153, s[16:17]
	v_cndmask_b32_e64 v87, v87, v153, s[18:19]
	v_cndmask_b32_e64 v88, v88, v153, s[20:21]
	v_cndmask_b32_e64 v89, v89, v153, s[22:23]
	v_cndmask_b32_e64 v90, v90, v153, s[24:25]
	v_cndmask_b32_e64 v91, v91, v153, s[26:27]
	v_cndmask_b32_e64 v92, v92, v153, s[28:29]
	v_cndmask_b32_e64 v93, v93, v153, s[30:31]
	v_cndmask_b32_e64 v94, v94, v153, s[34:35]
	v_cndmask_b32_e64 v95, v95, v153, s[36:37]
	v_cndmask_b32_e64 v96, v96, v153, s[38:39]
	v_cndmask_b32_e64 v97, v97, v153, s[40:41]
	s_waitcnt vmcnt(13) lgkmcnt(1)
	s_nop 0
	v_mfma_f32_32x32x16_bf16 v[82:97], v[4:7], v[126:129], v[82:97]
	ds_read_b128 v[4:7], v12 offset:64
	s_waitcnt lgkmcnt(1)
	v_mfma_f32_32x32x16_bf16 v[82:97], v[8:11], v[122:125], v[82:97]
	s_waitcnt lgkmcnt(0)
	v_mfma_f32_32x32x16_bf16 v[82:97], v[4:7], v[118:121], v[82:97]
	ds_read_b128 v[4:7], v12 offset:96
	s_waitcnt vmcnt(12) lgkmcnt(0)
	v_mfma_f32_32x32x16_bf16 v[82:97], v[4:7], v[114:117], v[82:97]
	s_nop 15
	s_nop 7
	s_nop 0
	v_max3_f32 v3, v82, v83, v84
	v_max3_f32 v4, v85, v86, v87
	v_max3_f32 v5, v88, v89, v90
	v_max3_f32 v6, v91, v92, v93
	v_max3_f32 v7, v94, v95, v96
	s_nop 0
	v_max3_f32 v3, v3, v4, v97
	v_max3_f32 v4, v5, v6, v7
	s_nop 0
	v_max_f32 v3, v3, v4
	s_nop 0
	v_mov_b32_e32 v4, v3
	s_nop 1
	v_permlane32_swap_b32_e32 v3, v4
	v_max_f32_e32 v4, v4, v4
	v_max_f32_e32 v3, v3, v3
	v_max_f32_e32 v3, v3, v4
	v_cmp_lt_f32_e32 vcc, s63, v3
	s_cbranch_vccz .LBB0_906
	s_nop 0
	v_cndmask_b32_e32 v4, 0, v3, vcc
	v_exp_f32_e64 v6, -v4
	v_add_f32_e32 v1, v1, v4
	v_pk_add_f32 v[82:83], v[82:83], v[4:5] op_sel_hi:[1,0] neg_lo:[0,1] neg_hi:[0,1]
	v_pk_add_f32 v[84:85], v[84:85], v[4:5] op_sel_hi:[1,0] neg_lo:[0,1] neg_hi:[0,1]
	v_mul_f32_e32 v160, v160, v6
	v_pk_add_f32 v[86:87], v[86:87], v[4:5] op_sel_hi:[1,0] neg_lo:[0,1] neg_hi:[0,1]
	v_pk_add_f32 v[88:89], v[88:89], v[4:5] op_sel_hi:[1,0] neg_lo:[0,1] neg_hi:[0,1]
	v_pk_add_f32 v[90:91], v[90:91], v[4:5] op_sel_hi:[1,0] neg_lo:[0,1] neg_hi:[0,1]
	v_pk_add_f32 v[92:93], v[92:93], v[4:5] op_sel_hi:[1,0] neg_lo:[0,1] neg_hi:[0,1]
	v_pk_add_f32 v[94:95], v[94:95], v[4:5] op_sel_hi:[1,0] neg_lo:[0,1] neg_hi:[0,1]
	v_pk_add_f32 v[96:97], v[96:97], v[4:5] op_sel_hi:[1,0] neg_lo:[0,1] neg_hi:[0,1]
	v_pk_mul_f32 v[80:81], v[80:81], v[6:7] op_sel_hi:[1,0]
	v_pk_mul_f32 v[78:79], v[78:79], v[6:7] op_sel_hi:[1,0]
	v_pk_mul_f32 v[76:77], v[76:77], v[6:7] op_sel_hi:[1,0]
	v_pk_mul_f32 v[74:75], v[74:75], v[6:7] op_sel_hi:[1,0]
	v_pk_mul_f32 v[72:73], v[72:73], v[6:7] op_sel_hi:[1,0]
	v_pk_mul_f32 v[70:71], v[70:71], v[6:7] op_sel_hi:[1,0]
	v_pk_mul_f32 v[68:69], v[68:69], v[6:7] op_sel_hi:[1,0]
	v_pk_mul_f32 v[66:67], v[66:67], v[6:7] op_sel_hi:[1,0]
	v_pk_mul_f32 v[64:65], v[64:65], v[6:7] op_sel_hi:[1,0]
	v_pk_mul_f32 v[62:63], v[62:63], v[6:7] op_sel_hi:[1,0]
	v_pk_mul_f32 v[60:61], v[60:61], v[6:7] op_sel_hi:[1,0]
	v_pk_mul_f32 v[58:59], v[58:59], v[6:7] op_sel_hi:[1,0]
	v_pk_mul_f32 v[56:57], v[56:57], v[6:7] op_sel_hi:[1,0]
	v_pk_mul_f32 v[54:55], v[54:55], v[6:7] op_sel_hi:[1,0]
	v_pk_mul_f32 v[52:53], v[52:53], v[6:7] op_sel_hi:[1,0]
	v_pk_mul_f32 v[50:51], v[50:51], v[6:7] op_sel_hi:[1,0]
	s_branch .LBB0_906

; __device__ __forceinline__ void swa_unit(Frame& F, const bf16_t* proj, const float* sinks, unsigned char* Y, int b, int kvh, int qb) {
;     ...
;     for (int sb = 0; sb < 4; ++sb) {
;         const int t = qb * 128 + sb * 32 + r32;
;         bf16x8 qf[4];
;         { const bf16_t* qrow = proj + (rb + t) * NIN + C_SQ + hq * 64 + hh * 8;
; #pragma unroll
;           for (int s = 0; s < 4; ++s) qf[s] = *(const bf16x8*)(qrow + s * 16); }
;         State st; init(st);
;         int kt0 = sb; if (qb == 0 && kt0 < 4) kt0 = 4;
;         if (kt0 == sb) tile<2>(lds, sb, qf, st, lane);
.LBB0_2016:
	s_lshl_b32 s77, s76, 5
	v_add_u32_e32 v3, s77, v154
	v_or_b32_e32 v146, s54, v3
	v_mov_b64_e32 v[4:5], s[58:59]
	v_mad_u64_u32 v[4:5], s[52:53], v146, s56, v[4:5]
	v_mad_i32_i24 v5, s55, v151, v5
	v_lshl_add_u64 v[4:5], v[4:5], 0, s[0:1]
	v_lshl_add_u64 v[4:5], v[140:141], 1, v[4:5]
	v_lshl_add_u64 v[6:7], v[4:5], 0, s[44:45]
	v_add_co_u32_e32 v4, vcc, 0x1000, v4
	s_and_b64 s[52:53], exec, s[46:47]
	s_nop 0
	v_addc_co_u32_e32 v5, vcc, 0, v5, vcc
	s_cselect_b32 s78, 4, s76
	s_cmp_lg_u32 s76, 0
	s_cbranch_scc1 .Lswq0_sel
	global_load_dwordx4 v[122:125], v[6:7], off offset:32
	global_load_dwordx4 v[114:117], v[6:7], off offset:64
	global_load_dwordx4 v[126:129], v[4:5], off offset:3072
	global_load_dwordx4 v[118:121], v[6:7], off offset:96
	s_mov_b64 s[52:53], 0x4c000
	v_lshl_add_u64 v[200:201], v[6:7], 0, s[52:53]
	v_lshl_add_u64 v[234:235], v[4:5], 0, s[52:53]
	global_load_dwordx4 v[186:189], v[200:201], off offset:32
	global_load_dwordx4 v[190:193], v[200:201], off offset:64
	global_load_dwordx4 v[196:199], v[234:235], off offset:3072
	global_load_dwordx4 v[210:213], v[200:201], off offset:96
	s_add_u32 s52, s52, 0x4c000
	v_lshl_add_u64 v[200:201], v[6:7], 0, s[52:53]
	v_lshl_add_u64 v[234:235], v[4:5], 0, s[52:53]
	global_load_dwordx4 v[214:217], v[200:201], off offset:32
	global_load_dwordx4 v[218:221], v[200:201], off offset:64
	global_load_dwordx4 v[222:225], v[234:235], off offset:3072
	global_load_dwordx4 v[230:233], v[200:201], off offset:96
	s_add_u32 s52, s52, 0x4c000
	v_lshl_add_u64 v[200:201], v[6:7], 0, s[52:53]
	v_lshl_add_u64 v[234:235], v[4:5], 0, s[52:53]
	global_load_dwordx4 v[238:241], v[200:201], off offset:32
	global_load_dwordx4 v[242:245], v[200:201], off offset:64
	global_load_dwordx4 v[246:249], v[234:235], off offset:3072
	global_load_dwordx4 v[250:253], v[200:201], off offset:96
	s_branch .Lswq0_done
.Lswq0_sel:
	s_waitcnt vmcnt(4)
	s_cmp_eq_u32 s76, 1
	s_cbranch_scc0 .Lswq0_c2
	v_mov_b64_e32 v[122:123], v[186:187]
	v_mov_b64_e32 v[124:125], v[188:189]
	v_mov_b64_e32 v[114:115], v[190:191]
	v_mov_b64_e32 v[116:117], v[192:193]
	v_mov_b64_e32 v[126:127], v[196:197]
	v_mov_b64_e32 v[128:129], v[198:199]
	v_mov_b64_e32 v[118:119], v[210:211]
	v_mov_b64_e32 v[120:121], v[212:213]
	s_branch .Lswq0_done
.Lswq0_c2:
	s_cmp_eq_u32 s76, 2
	s_cbranch_scc0 .Lswq0_c3
	v_mov_b64_e32 v[122:123], v[214:215]
	v_mov_b64_e32 v[124:125], v[216:217]
	v_mov_b64_e32 v[114:115], v[218:219]
	v_mov_b64_e32 v[116:117], v[220:221]
	v_mov_b64_e32 v[126:127], v[222:223]
	v_mov_b64_e32 v[128:129], v[224:225]
	v_mov_b64_e32 v[118:119], v[230:231]
	v_mov_b64_e32 v[120:121], v[232:233]
	s_branch .Lswq0_done
.Lswq0_c3:
	v_mov_b64_e32 v[122:123], v[238:239]
	v_mov_b64_e32 v[124:125], v[240:241]
	v_mov_b64_e32 v[114:115], v[242:243]
	v_mov_b64_e32 v[116:117], v[244:245]
	v_mov_b64_e32 v[126:127], v[246:247]
	v_mov_b64_e32 v[128:129], v[248:249]
	v_mov_b64_e32 v[118:119], v[250:251]
	v_mov_b64_e32 v[120:121], v[252:253]
.Lswq0_done:
	v_mov_b32_e32 v147, s55
	s_cmp_eq_u32 s78, s76
	s_mov_b64 s[52:53], -1
	s_cbranch_scc1 .LBB0_2018
	s_mov_b64 s[52:53], 0
.LBB0_2018:
	s_andn2_b64 vcc, exec, s[52:53]
	s_cbranch_vccnz .LBB0_2021
	v_or_b32_e32 v3, s77, v139
	v_mad_u64_u32 v[12:13], s[52:53], v3, s57, v[142:143]
	ds_read_b128 v[4:7], v12
	ds_read_b128 v[8:11], v12 offset:32
	s_waitcnt vmcnt(13) lgkmcnt(1)
	v_mfma_f32_32x32x16_bf16 v[66:81], v[4:7], v[126:129], v[34:49]
	s_waitcnt lgkmcnt(0)
	v_mfma_f32_32x32x16_bf16 v[66:81], v[8:11], v[122:125], v[66:81]
	ds_read_b128 v[4:7], v12 offset:64
	ds_read_b128 v[8:11], v12 offset:96
	s_waitcnt lgkmcnt(1)
	v_mfma_f32_32x32x16_bf16 v[66:81], v[4:7], v[114:117], v[66:81]
	s_waitcnt vmcnt(12) lgkmcnt(0)
	v_mfma_f32_32x32x16_bf16 v[66:81], v[8:11], v[118:121], v[66:81]
	s_nop 15
	s_nop 7
	s_nop 0
	v_max3_f32 v3, v66, v67, v68
	v_max3_f32 v4, v69, v70, v71
	v_max3_f32 v5, v72, v73, v74
	v_max3_f32 v6, v75, v76, v77
	v_max3_f32 v7, v78, v79, v80
	s_nop 0
	v_max3_f32 v3, v3, v4, v81
	v_max3_f32 v4, v5, v6, v7
	s_nop 0
	v_max_f32 v3, v3, v4
	s_nop 0
	v_mov_b32_e32 v4, v3
	s_nop 1
	v_permlane32_swap_b32_e32 v3, v4
	v_max_f32_e32 v4, v4, v4
	v_max_f32_e32 v3, v3, v3
	v_max_f32_e32 v3, v3, v4
	v_cmp_lt_f32_e32 vcc, s68, v3
	s_cbranch_vccz .LBB0_2022
	s_nop 0
	v_cndmask_b32_e32 v4, 0, v3, vcc
	v_exp_f32_e64 v3, -v4
	v_sub_f32_e32 v82, 0x447a0000, v4
	v_add_f32_e32 v159, 0xc47a0000, v4
	v_pk_add_f32 v[66:67], v[66:67], v[4:5] op_sel_hi:[1,0] neg_lo:[0,1] neg_hi:[0,1]
	v_mul_f32_e32 v50, 0, v3
	v_pk_add_f32 v[68:69], v[68:69], v[4:5] op_sel_hi:[1,0] neg_lo:[0,1] neg_hi:[0,1]
	v_pk_add_f32 v[70:71], v[70:71], v[4:5] op_sel_hi:[1,0] neg_lo:[0,1] neg_hi:[0,1]
	v_pk_add_f32 v[72:73], v[72:73], v[4:5] op_sel_hi:[1,0] neg_lo:[0,1] neg_hi:[0,1]
	v_pk_add_f32 v[74:75], v[74:75], v[4:5] op_sel_hi:[1,0] neg_lo:[0,1] neg_hi:[0,1]
	v_pk_add_f32 v[76:77], v[76:77], v[4:5] op_sel_hi:[1,0] neg_lo:[0,1] neg_hi:[0,1]
	v_pk_add_f32 v[78:79], v[78:79], v[4:5] op_sel_hi:[1,0] neg_lo:[0,1] neg_hi:[0,1]
	v_pk_add_f32 v[80:81], v[80:81], v[4:5] op_sel_hi:[1,0] neg_lo:[0,1] neg_hi:[0,1]
	v_mov_b32_e32 v83, v82
	v_mov_b32_e32 v84, v82
	v_mov_b32_e32 v85, v82
	v_mov_b32_e32 v86, v82
	v_mov_b32_e32 v87, v82
	v_mov_b32_e32 v88, v82
	v_mov_b32_e32 v89, v82
	v_mov_b32_e32 v90, v82
	v_mov_b32_e32 v91, v82
	v_mov_b32_e32 v92, v82
	v_mov_b32_e32 v93, v82
	v_mov_b32_e32 v94, v82
	v_mov_b32_e32 v95, v82
	v_mov_b32_e32 v96, v82
	v_mov_b32_e32 v97, v82
	s_branch .LBB0_2023

; #define LAS __attribute__((address_space(3)))
; __device__ __forceinline__ float xhalf_max(float v) { auto rr = __builtin_amdgcn_permlane32_swap(__float_as_uint(v), __float_as_uint(v), false, false); return fmaxf(__uint_as_float(rr[0]), __uint_as_float(rr[1])); }
; template <int MODE>
; __device__ __forceinline__ void tile(LAS unsigned char* lds, int kt, const bf16x8 (&qf)[4], State& st, int lane) {
;     const int r32 = lane & 31, h = lane >> 5;
;     f32x16 S;
;     if (MODE == 3) S = st.negm;
;     else {
; #pragma unroll
;         for (int r = 0; r < 16; ++r) { const int ko = (r & 3) + 8 * (r >> 2) + 4 * h; const bool ok = (MODE == 1) ? (ko <= r32) : (ko > r32); S[r] = ok ? st.negm[r] : NEG; } }
;     const LAS unsigned char* kp = lds + K_OFF + (kt * 32 + r32) * KROW + h * 16;
; #pragma unroll
;     for (int s = 0; s < 4; ++s) { const bf16x8 a = *(const LAS bf16x8*)(kp + s * 32); S = __builtin_amdgcn_mfma_f32_32x32x16_bf16(a, qf[s], S, 0, 0, 0); }
;     float tmax;
;     asm volatile("s_nop 15\n\ts_nop 7" : "+v"(S));
;     { float m0, m1, m2, m3, m4;
;       asm("v_max3_f32 %0, %1, %2, %3" : "=v"(m0) : "v"(S[0]), "v"(S[1]), "v"(S[2]));    asm("v_max3_f32 %0, %1, %2, %3" : "=v"(m1) : "v"(S[3]), "v"(S[4]), "v"(S[5]));
;       asm("v_max3_f32 %0, %1, %2, %3" : "=v"(m2) : "v"(S[6]), "v"(S[7]), "v"(S[8]));    asm("v_max3_f32 %0, %1, %2, %3" : "=v"(m3) : "v"(S[9]), "v"(S[10]), "v"(S[11]));
;       asm("v_max3_f32 %0, %1, %2, %3" : "=v"(m4) : "v"(S[12]), "v"(S[13]), "v"(S[14])); asm("v_max3_f32 %0, %1, %2, %3" : "=v"(m0) : "v"(m0), "v"(m1), "v"(S[15]));
;       asm("v_max3_f32 %0, %1, %2, %3" : "=v"(m2) : "v"(m2), "v"(m3), "v"(m4));          asm("v_max_f32 %0, %1, %2" : "=v"(tmax) : "v"(m0), "v"(m2)); }
;     tmax = xhalf_max(tmax);
;     if (__any(tmax > THR)) {
;         const float d = tmax > THR ? tmax : 0.f, alpha = __builtin_amdgcn_exp2f(-d);
;         st.m += d; st.l *= alpha;
; #pragma unroll
;         for (int r = 0; r < 16; ++r) { S[r] -= d; st.negm[r] -= d; st.o0[r] *= alpha; st.o1[r] *= alpha; }
;     }
.LBB0_2027:
	ds_read_b128 v[6:9], v4
	ds_read_b128 v[10:13], v4 offset:32
	s_waitcnt vmcnt(13) lgkmcnt(1)
	v_mfma_f32_32x32x16_bf16 v[98:113], v[6:9], v[126:129], v[82:97]
	s_waitcnt lgkmcnt(0)
	v_mfma_f32_32x32x16_bf16 v[98:113], v[10:13], v[122:125], v[98:113]
	ds_read_b128 v[6:9], v4 offset:64
	ds_read_b128 v[10:13], v4 offset:96
	s_waitcnt lgkmcnt(1)
	v_mfma_f32_32x32x16_bf16 v[98:113], v[6:9], v[114:117], v[98:113]
	s_waitcnt vmcnt(12) lgkmcnt(0)
	v_mfma_f32_32x32x16_bf16 v[98:113], v[10:13], v[118:121], v[98:113]
	s_nop 15
	s_nop 7
	s_nop 0
	v_max3_f32 v5, v98, v99, v100
	v_max3_f32 v6, v101, v102, v103
	v_max3_f32 v7, v104, v105, v106
	v_max3_f32 v8, v107, v108, v109
	v_max3_f32 v9, v110, v111, v112
	s_nop 0
	v_max3_f32 v5, v5, v6, v113
	v_max3_f32 v6, v7, v8, v9
	s_nop 0
	v_max_f32 v5, v5, v6
	s_nop 0
	v_mov_b32_e32 v6, v5
	s_nop 1
	v_permlane32_swap_b32_e32 v5, v6
	v_max_f32_e32 v6, v6, v6
	v_max_f32_e32 v5, v5, v5
	v_max_f32_e32 v5, v5, v6
	v_cmp_lt_f32_e32 vcc, s68, v5
	s_cbranch_vccz .LBB0_2026
	s_nop 0
	v_cndmask_b32_e32 v6, 0, v5, vcc
	v_exp_f32_e64 v8, -v6
	v_add_f32_e32 v159, v159, v6
	v_pk_add_f32 v[98:99], v[98:99], v[6:7] op_sel_hi:[1,0] neg_lo:[0,1] neg_hi:[0,1]
	v_pk_add_f32 v[100:101], v[100:101], v[6:7] op_sel_hi:[1,0] neg_lo:[0,1] neg_hi:[0,1]
	v_mul_f32_e32 v160, v160, v8
	v_pk_add_f32 v[102:103], v[102:103], v[6:7] op_sel_hi:[1,0] neg_lo:[0,1] neg_hi:[0,1]
	v_pk_add_f32 v[104:105], v[104:105], v[6:7] op_sel_hi:[1,0] neg_lo:[0,1] neg_hi:[0,1]
	v_pk_add_f32 v[106:107], v[106:107], v[6:7] op_sel_hi:[1,0] neg_lo:[0,1] neg_hi:[0,1]
	v_pk_add_f32 v[108:109], v[108:109], v[6:7] op_sel_hi:[1,0] neg_lo:[0,1] neg_hi:[0,1]
	v_pk_add_f32 v[110:111], v[110:111], v[6:7] op_sel_hi:[1,0] neg_lo:[0,1] neg_hi:[0,1]
	v_pk_add_f32 v[112:113], v[112:113], v[6:7] op_sel_hi:[1,0] neg_lo:[0,1] neg_hi:[0,1]
	v_sub_f32_e32 v97, v97, v6
	v_sub_f32_e32 v96, v96, v6
	v_sub_f32_e32 v95, v95, v6
	v_sub_f32_e32 v94, v94, v6
	v_sub_f32_e32 v93, v93, v6
	v_sub_f32_e32 v92, v92, v6
	v_sub_f32_e32 v91, v91, v6
	v_sub_f32_e32 v90, v90, v6
	v_sub_f32_e32 v89, v89, v6
	v_sub_f32_e32 v88, v88, v6
	v_sub_f32_e32 v87, v87, v6
	v_sub_f32_e32 v86, v86, v6
	v_sub_f32_e32 v85, v85, v6
	v_sub_f32_e32 v84, v84, v6
	v_sub_f32_e32 v83, v83, v6
	v_sub_f32_e32 v82, v82, v6
	v_pk_mul_f32 v[80:81], v[80:81], v[8:9] op_sel_hi:[1,0]
	v_pk_mul_f32 v[78:79], v[78:79], v[8:9] op_sel_hi:[1,0]
	v_pk_mul_f32 v[76:77], v[76:77], v[8:9] op_sel_hi:[1,0]
	v_pk_mul_f32 v[74:75], v[74:75], v[8:9] op_sel_hi:[1,0]
	v_pk_mul_f32 v[72:73], v[72:73], v[8:9] op_sel_hi:[1,0]
	v_pk_mul_f32 v[70:71], v[70:71], v[8:9] op_sel_hi:[1,0]
	v_pk_mul_f32 v[68:69], v[68:69], v[8:9] op_sel_hi:[1,0]
	v_pk_mul_f32 v[66:67], v[66:67], v[8:9] op_sel_hi:[1,0]
	v_pk_mul_f32 v[64:65], v[64:65], v[8:9] op_sel_hi:[1,0]
	v_pk_mul_f32 v[62:63], v[62:63], v[8:9] op_sel_hi:[1,0]
	v_pk_mul_f32 v[60:61], v[60:61], v[8:9] op_sel_hi:[1,0]
	v_pk_mul_f32 v[58:59], v[58:59], v[8:9] op_sel_hi:[1,0]
	v_pk_mul_f32 v[56:57], v[56:57], v[8:9] op_sel_hi:[1,0]
	v_pk_mul_f32 v[54:55], v[54:55], v[8:9] op_sel_hi:[1,0]
	v_pk_mul_f32 v[52:53], v[52:53], v[8:9] op_sel_hi:[1,0]
	v_pk_mul_f32 v[50:51], v[50:51], v[8:9] op_sel_hi:[1,0]
	s_branch .LBB0_2026
.LBB0_2029:
	v_lshl_or_b32 v3, s53, 5, v139
	v_mad_u64_u32 v[12:13], s[76:77], v3, s57, v[142:143]
	ds_read_b128 v[4:7], v12
	ds_read_b128 v[8:11], v12 offset:32
	v_cndmask_b32_e64 v82, v82, v152, s[8:9]
	v_cndmask_b32_e64 v83, v152, v83, s[10:11]
	v_cndmask_b32_e64 v84, v84, v152, s[38:39]
	v_cndmask_b32_e64 v85, v85, v152, s[40:41]
	v_cndmask_b32_e64 v86, v86, v152, s[12:13]
	v_cndmask_b32_e64 v87, v87, v152, s[14:15]
	v_cndmask_b32_e64 v88, v88, v152, s[16:17]
	v_cndmask_b32_e64 v89, v89, v152, s[18:19]
	v_cndmask_b32_e64 v90, v90, v152, s[20:21]
	v_cndmask_b32_e64 v91, v91, v152, s[22:23]
	v_cndmask_b32_e64 v92, v92, v152, s[24:25]
	v_cndmask_b32_e64 v93, v93, v152, s[26:27]
	v_cndmask_b32_e64 v94, v94, v152, s[28:29]
	v_cndmask_b32_e64 v95, v95, v152, s[30:31]
	v_cndmask_b32_e64 v96, v96, v152, s[34:35]
	v_cndmask_b32_e64 v97, v97, v152, s[36:37]
	s_waitcnt vmcnt(13) lgkmcnt(1)
	s_nop 0
	v_mfma_f32_32x32x16_bf16 v[82:97], v[4:7], v[126:129], v[82:97]
	s_waitcnt lgkmcnt(0)
	v_mfma_f32_32x32x16_bf16 v[82:97], v[8:11], v[122:125], v[82:97]
	ds_read_b128 v[4:7], v12 offset:64
	ds_read_b128 v[8:11], v12 offset:96
	s_waitcnt lgkmcnt(1)
	v_mfma_f32_32x32x16_bf16 v[82:97], v[4:7], v[114:117], v[82:97]
	s_waitcnt vmcnt(12) lgkmcnt(0)
	v_mfma_f32_32x32x16_bf16 v[82:97], v[8:11], v[118:121], v[82:97]
	s_nop 15
	s_nop 7
	s_nop 0
	v_max3_f32 v3, v82, v83, v84
	v_max3_f32 v4, v85, v86, v87
	v_max3_f32 v5, v88, v89, v90
	v_max3_f32 v6, v91, v92, v93
	v_max3_f32 v7, v94, v95, v96
	s_nop 0
	v_max3_f32 v3, v3, v4, v97
	v_max3_f32 v4, v5, v6, v7
	s_nop 0
	v_max_f32 v3, v3, v4
	s_nop 0
	v_mov_b32_e32 v4, v3
	s_nop 1
	v_permlane32_swap_b32_e32 v3, v4
	v_max_f32_e32 v4, v4, v4
	v_max_f32_e32 v3, v3, v3
	v_max_f32_e32 v3, v3, v4
	v_cmp_lt_f32_e32 vcc, s68, v3
	s_cbranch_vccz .LBB0_2015
	s_nop 0
	v_cndmask_b32_e32 v4, 0, v3, vcc
	v_exp_f32_e64 v6, -v4
	v_add_f32_e32 v159, v159, v4
	v_pk_add_f32 v[82:83], v[82:83], v[4:5] op_sel_hi:[1,0] neg_lo:[0,1] neg_hi:[0,1]
	v_pk_add_f32 v[84:85], v[84:85], v[4:5] op_sel_hi:[1,0] neg_lo:[0,1] neg_hi:[0,1]
	v_mul_f32_e32 v160, v160, v6
	v_pk_add_f32 v[86:87], v[86:87], v[4:5] op_sel_hi:[1,0] neg_lo:[0,1] neg_hi:[0,1]
	v_pk_add_f32 v[88:89], v[88:89], v[4:5] op_sel_hi:[1,0] neg_lo:[0,1] neg_hi:[0,1]
	v_pk_add_f32 v[90:91], v[90:91], v[4:5] op_sel_hi:[1,0] neg_lo:[0,1] neg_hi:[0,1]
	v_pk_add_f32 v[92:93], v[92:93], v[4:5] op_sel_hi:[1,0] neg_lo:[0,1] neg_hi:[0,1]
	v_pk_add_f32 v[94:95], v[94:95], v[4:5] op_sel_hi:[1,0] neg_lo:[0,1] neg_hi:[0,1]
	v_pk_add_f32 v[96:97], v[96:97], v[4:5] op_sel_hi:[1,0] neg_lo:[0,1] neg_hi:[0,1]
	v_pk_mul_f32 v[80:81], v[80:81], v[6:7] op_sel_hi:[1,0]
	v_pk_mul_f32 v[78:79], v[78:79], v[6:7] op_sel_hi:[1,0]
	v_pk_mul_f32 v[76:77], v[76:77], v[6:7] op_sel_hi:[1,0]
	v_pk_mul_f32 v[74:75], v[74:75], v[6:7] op_sel_hi:[1,0]
	v_pk_mul_f32 v[72:73], v[72:73], v[6:7] op_sel_hi:[1,0]
	v_pk_mul_f32 v[70:71], v[70:71], v[6:7] op_sel_hi:[1,0]
	v_pk_mul_f32 v[68:69], v[68:69], v[6:7] op_sel_hi:[1,0]
	v_pk_mul_f32 v[66:67], v[66:67], v[6:7] op_sel_hi:[1,0]
	v_pk_mul_f32 v[64:65], v[64:65], v[6:7] op_sel_hi:[1,0]
	v_pk_mul_f32 v[62:63], v[62:63], v[6:7] op_sel_hi:[1,0]
	v_pk_mul_f32 v[60:61], v[60:61], v[6:7] op_sel_hi:[1,0]
	v_pk_mul_f32 v[58:59], v[58:59], v[6:7] op_sel_hi:[1,0]
	v_pk_mul_f32 v[56:57], v[56:57], v[6:7] op_sel_hi:[1,0]
	v_pk_mul_f32 v[54:55], v[54:55], v[6:7] op_sel_hi:[1,0]
	v_pk_mul_f32 v[52:53], v[52:53], v[6:7] op_sel_hi:[1,0]
	v_pk_mul_f32 v[50:51], v[50:51], v[6:7] op_sel_hi:[1,0]
	s_branch .LBB0_2015
